# grid barrier: every workgroup, XCD leaders included, is released by polling the top-level arrival counter (non-returning add, target = (generation+1) x XCDs)
# speedup vs baseline: 1.0040x; 1.0004x over previous
; __device__ __forceinline__ unsigned xb_ld(unsigned* p)              { return __hip_atomic_load(p, __ATOMIC_RELAXED, __HIP_MEMORY_SCOPE_AGENT); }
; __device__ __forceinline__ unsigned xb_add(unsigned* p, unsigned v) { return __hip_atomic_fetch_add(p, v, __ATOMIC_RELAXED, __HIP_MEMORY_SCOPE_AGENT); }
; #define XB_SPIN(cond, bar) do { unsigned _sp = 0; while (cond) { __builtin_amdgcn_s_sleep(1); \
;     if ((++_sp & 255u) == 0u) { if (xb_ld(&(bar)[XB_TMO])) break; if (_sp > XB_SPIN_CAP) { atomicAdd(&(bar)[XB_TMO], 1u); break; } } } } while (0)
; __device__ __forceinline__ void xcd_barrier(const XcdBarrier& b) {
;     asm volatile("s_waitcnt vmcnt(0)" ::: "memory");
;     __syncthreads();
;     if (threadIdx.x == 0) {
;         unsigned* bar = b.bar;
;         __builtin_amdgcn_s_waitcnt(0);
;         unsigned nloc = b.st[0], nx = b.st[1];
;         if (nloc == 0u) { xcd_barrier_complete(bar, b.x, b.total, nloc, nx); b.st[0] = nloc; b.st[1] = nx; }
;         const unsigned old = xb_add(&bar[XB_XSUB(b.x)], 1u);
;         const unsigned gen = old / nloc;
;         if (old + 1u == (gen + 1u) * nloc) {
;             __builtin_amdgcn_fence(__ATOMIC_RELEASE, "agent");
;             asm volatile("s_waitcnt vmcnt(0)" ::: "memory");
;             const unsigned og = xb_add(&bar[XB_TOP], 1u);
;             const unsigned tg = og / nx;
;             if (og + 1u == (tg + 1u) * nx) xb_add(&bar[XB_TOPGEN], 1u);
;             else XB_SPIN(xb_ld(&bar[XB_TOPGEN]) == tg, bar);
;             __builtin_amdgcn_fence(__ATOMIC_ACQUIRE, "agent");
;             xb_add(&bar[XB_XGEN(b.x)], 1u);
;             asm volatile("s_waitcnt vmcnt(0)" ::: "memory");
;         } else {
;             XB_SPIN(xb_ld(&bar[XB_XGEN(b.x)]) == gen, bar);
.LBB0_81:
	s_or_b64 exec, exec, s[10:11]
	v_cvt_f32_u32_e32 v5, v3
	s_waitcnt vmcnt(0)
	v_readfirstlane_b32 s0, v4
	v_sub_u32_e32 v4, 0, v3
	v_rcp_iflag_f32_e32 v5, v5
	v_add_u32_e32 v6, s0, v2
	v_mul_f32_e32 v5, 0x4f7ffffe, v5
	v_cvt_u32_f32_e32 v5, v5
	v_mul_lo_u32 v2, v4, v5
	v_mul_hi_u32 v2, v5, v2
	v_add_u32_e32 v2, v5, v2
	v_mul_hi_u32 v2, v6, v2
	v_mul_lo_u32 v4, v2, v3
	v_sub_u32_e32 v4, v6, v4
	v_add_u32_e32 v5, 1, v2
	v_cmp_ge_u32_e32 vcc, v4, v3
	s_nop 1
	v_cndmask_b32_e32 v2, v2, v5, vcc
	v_sub_u32_e32 v5, v4, v3
	v_cndmask_b32_e32 v4, v4, v5, vcc
	v_add_u32_e32 v5, 1, v2
	v_cmp_ge_u32_e32 vcc, v4, v3
	v_add_u32_e32 v4, 1, v6
	s_nop 0
	v_cndmask_b32_e32 v2, v2, v5, vcc
	v_mul_lo_u32 v5, v3, v2
	v_add_u32_e32 v3, v5, v3
	v_cmp_ne_u32_e32 vcc, v4, v3
	s_and_saveexec_b64 s[0:1], vcc
	s_xor_b64 s[10:11], exec, s[0:1]
	s_cbranch_execz .LBB0_95
	s_waitcnt lgkmcnt(0)
	v_add_u32_e32 v4, 1, v2
	v_mul_lo_u32 v4, v4, v1
	v_mov_b32_e32 v1, 0x3000
	global_load_dword v1, v1, s[42:43] offset:1024 sc1
	s_add_u32 s12, s42, 0x3400
	s_addc_u32 s13, s43, 0
	s_waitcnt vmcnt(0)
	v_cmp_lt_u32_e32 vcc, v1, v4
	s_and_saveexec_b64 s[0:1], vcc
	s_cbranch_execz .LBB0_94
	s_mov_b32 s28, 1
	s_mov_b64 s[14:15], 0
	v_mov_b32_e32 v1, 0
	s_branch .LBB0_85

; __device__ __forceinline__ unsigned xb_ld(unsigned* p)              { return __hip_atomic_load(p, __ATOMIC_RELAXED, __HIP_MEMORY_SCOPE_AGENT); }
; #define XB_SPIN(cond, bar) do { unsigned _sp = 0; while (cond) { __builtin_amdgcn_s_sleep(1); \
;     if ((++_sp & 255u) == 0u) { if (xb_ld(&(bar)[XB_TMO])) break; if (_sp > XB_SPIN_CAP) { atomicAdd(&(bar)[XB_TMO], 1u); break; } } } } while (0)
; __device__ __forceinline__ void xcd_barrier(const XcdBarrier& b) {
;     ...
;             XB_SPIN(xb_ld(&bar[XB_XGEN(b.x)]) == gen, bar);
.LBB0_87:
	global_load_dword v3, v1, s[12:13] sc1
	s_add_i32 s28, s28, 1
	s_mov_b64 s[20:21], -1
	s_waitcnt vmcnt(0)
	v_cmp_ge_u32_e32 vcc, v3, v4
	s_orn2_b64 s[18:19], vcc, exec
	s_branch .LBB0_84

; __device__ __forceinline__ unsigned xb_ld(unsigned* p)              { return __hip_atomic_load(p, __ATOMIC_RELAXED, __HIP_MEMORY_SCOPE_AGENT); }
; __device__ __forceinline__ unsigned xb_add(unsigned* p, unsigned v) { return __hip_atomic_fetch_add(p, v, __ATOMIC_RELAXED, __HIP_MEMORY_SCOPE_AGENT); }
; #define XB_SPIN(cond, bar) do { unsigned _sp = 0; while (cond) { __builtin_amdgcn_s_sleep(1); \
;     if ((++_sp & 255u) == 0u) { if (xb_ld(&(bar)[XB_TMO])) break; if (_sp > XB_SPIN_CAP) { atomicAdd(&(bar)[XB_TMO], 1u); break; } } } } while (0)
; __device__ __forceinline__ void xcd_barrier(const XcdBarrier& b) {
;     ...
;         if (old + 1u == (gen + 1u) * nloc) {
;             __builtin_amdgcn_fence(__ATOMIC_RELEASE, "agent");
;             asm volatile("s_waitcnt vmcnt(0)" ::: "memory");
;             const unsigned og = xb_add(&bar[XB_TOP], 1u);
;             const unsigned tg = og / nx;
;             if (og + 1u == (tg + 1u) * nx) xb_add(&bar[XB_TOPGEN], 1u);
;             else XB_SPIN(xb_ld(&bar[XB_TOPGEN]) == tg, bar);
;             __builtin_amdgcn_fence(__ATOMIC_ACQUIRE, "agent");
;             xb_add(&bar[XB_XGEN(b.x)], 1u);
;             asm volatile("s_waitcnt vmcnt(0)" ::: "memory");
.LBB0_95:
	s_andn2_saveexec_b64 s[0:1], s[10:11]
	s_cbranch_execz .LBB0_115
	s_mov_b64 s[0:1], exec
	v_add_u32_e32 v7, 1, v2
	buffer_wbl2 sc1
	s_waitcnt lgkmcnt(0)
	v_mul_lo_u32 v7, v7, v1
	s_waitcnt vmcnt(0)
	v_mbcnt_lo_u32_b32 v2, s0, 0
	v_mbcnt_hi_u32_b32 v2, s1, v2
	v_cmp_eq_u32_e32 vcc, 0, v2
	s_and_saveexec_b64 s[10:11], vcc
	s_cbranch_execz .LBB0_98
	s_bcnt1_i32_b64 s0, s[0:1]
	v_mov_b32_e32 v3, 0x3000
	v_mov_b32_e32 v4, s0
	global_atomic_add v3, v4, s[42:43] offset:1024
.LBB0_98:
	s_or_b64 exec, exec, s[10:11]
	v_mov_b32_e32 v1, 0
	v_mov_b32_e32 v5, 0
	s_add_u32 s0, s42, 0x3400
	s_addc_u32 s1, s43, 0
.Lxb_spin_0:
	global_load_dword v2, v1, s[0:1] sc1
	v_add_u32_e32 v5, 1, v5
	s_waitcnt vmcnt(0)
	v_cmp_ge_u32_e32 vcc, v2, v7
	s_cbranch_vccnz .Lxb_done_0
	v_cmp_lt_u32_e32 vcc, 0xfffff, v5
	s_cbranch_vccnz .Lxb_done_0
	s_sleep 1
	s_branch .Lxb_spin_0
.Lxb_done_0:
	buffer_inv sc1
	s_waitcnt vmcnt(0)

; __device__ __forceinline__ unsigned xb_ld(unsigned* p)              { return __hip_atomic_load(p, __ATOMIC_RELAXED, __HIP_MEMORY_SCOPE_AGENT); }
; __device__ __forceinline__ unsigned xb_add(unsigned* p, unsigned v) { return __hip_atomic_fetch_add(p, v, __ATOMIC_RELAXED, __HIP_MEMORY_SCOPE_AGENT); }
; #define XB_SPIN(cond, bar) do { unsigned _sp = 0; while (cond) { __builtin_amdgcn_s_sleep(1); \
;     if ((++_sp & 255u) == 0u) { if (xb_ld(&(bar)[XB_TMO])) break; if (_sp > XB_SPIN_CAP) { atomicAdd(&(bar)[XB_TMO], 1u); break; } } } } while (0)
; __device__ __forceinline__ void xcd_barrier(const XcdBarrier& b) {
;     asm volatile("s_waitcnt vmcnt(0)" ::: "memory");
;     __syncthreads();
;     if (threadIdx.x == 0) {
;         unsigned* bar = b.bar;
;         __builtin_amdgcn_s_waitcnt(0);
;         unsigned nloc = b.st[0], nx = b.st[1];
;         if (nloc == 0u) { xcd_barrier_complete(bar, b.x, b.total, nloc, nx); b.st[0] = nloc; b.st[1] = nx; }
;         const unsigned old = xb_add(&bar[XB_XSUB(b.x)], 1u);
;         const unsigned gen = old / nloc;
;         if (old + 1u == (gen + 1u) * nloc) {
;             __builtin_amdgcn_fence(__ATOMIC_RELEASE, "agent");
;             asm volatile("s_waitcnt vmcnt(0)" ::: "memory");
;             const unsigned og = xb_add(&bar[XB_TOP], 1u);
;             const unsigned tg = og / nx;
;             if (og + 1u == (tg + 1u) * nx) xb_add(&bar[XB_TOPGEN], 1u);
;             else XB_SPIN(xb_ld(&bar[XB_TOPGEN]) == tg, bar);
;             __builtin_amdgcn_fence(__ATOMIC_ACQUIRE, "agent");
;             xb_add(&bar[XB_XGEN(b.x)], 1u);
;             asm volatile("s_waitcnt vmcnt(0)" ::: "memory");
;         } else {
;             XB_SPIN(xb_ld(&bar[XB_XGEN(b.x)]) == gen, bar);
.LBB0_159:
	s_or_b64 exec, exec, s[10:11]
	v_cvt_f32_u32_e32 v5, v3
	s_waitcnt vmcnt(0)
	v_readfirstlane_b32 s0, v4
	v_sub_u32_e32 v4, 0, v3
	v_rcp_iflag_f32_e32 v5, v5
	v_add_u32_e32 v6, s0, v2
	v_mul_f32_e32 v5, 0x4f7ffffe, v5
	v_cvt_u32_f32_e32 v5, v5
	v_mul_lo_u32 v2, v4, v5
	v_mul_hi_u32 v2, v5, v2
	v_add_u32_e32 v2, v5, v2
	v_mul_hi_u32 v2, v6, v2
	v_mul_lo_u32 v4, v2, v3
	v_sub_u32_e32 v4, v6, v4
	v_add_u32_e32 v5, 1, v2
	v_cmp_ge_u32_e32 vcc, v4, v3
	s_nop 1
	v_cndmask_b32_e32 v2, v2, v5, vcc
	v_sub_u32_e32 v5, v4, v3
	v_cndmask_b32_e32 v4, v4, v5, vcc
	v_add_u32_e32 v5, 1, v2
	v_cmp_ge_u32_e32 vcc, v4, v3
	v_add_u32_e32 v4, 1, v6
	s_nop 0
	v_cndmask_b32_e32 v2, v2, v5, vcc
	v_mul_lo_u32 v5, v3, v2
	v_add_u32_e32 v3, v5, v3
	v_cmp_ne_u32_e32 vcc, v4, v3
	s_and_saveexec_b64 s[0:1], vcc
	s_xor_b64 s[10:11], exec, s[0:1]
	s_cbranch_execz .LBB0_173
	s_waitcnt lgkmcnt(0)
	v_add_u32_e32 v4, 1, v2
	v_mul_lo_u32 v4, v4, v1
	v_mov_b32_e32 v1, 0x3000
	global_load_dword v1, v1, s[42:43] offset:1024 sc1
	s_add_u32 s12, s42, 0x3400
	s_addc_u32 s13, s43, 0
	s_waitcnt vmcnt(0)
	v_cmp_lt_u32_e32 vcc, v1, v4
	s_and_saveexec_b64 s[0:1], vcc
	s_cbranch_execz .LBB0_172
	s_mov_b32 s3, 1
	s_mov_b64 s[14:15], 0
	v_mov_b32_e32 v1, 0
	s_branch .LBB0_163

; __device__ __forceinline__ unsigned xb_ld(unsigned* p)              { return __hip_atomic_load(p, __ATOMIC_RELAXED, __HIP_MEMORY_SCOPE_AGENT); }
; #define XB_SPIN(cond, bar) do { unsigned _sp = 0; while (cond) { __builtin_amdgcn_s_sleep(1); \
;     if ((++_sp & 255u) == 0u) { if (xb_ld(&(bar)[XB_TMO])) break; if (_sp > XB_SPIN_CAP) { atomicAdd(&(bar)[XB_TMO], 1u); break; } } } } while (0)
; __device__ __forceinline__ void xcd_barrier(const XcdBarrier& b) {
;     ...
;             XB_SPIN(xb_ld(&bar[XB_XGEN(b.x)]) == gen, bar);
.LBB0_165:
	global_load_dword v3, v1, s[12:13] sc1
	s_add_i32 s3, s3, 1
	s_mov_b64 s[20:21], -1
	s_waitcnt vmcnt(0)
	v_cmp_ge_u32_e32 vcc, v3, v4
	s_orn2_b64 s[18:19], vcc, exec
	s_branch .LBB0_162

; __device__ __forceinline__ unsigned xb_ld(unsigned* p)              { return __hip_atomic_load(p, __ATOMIC_RELAXED, __HIP_MEMORY_SCOPE_AGENT); }
; __device__ __forceinline__ unsigned xb_add(unsigned* p, unsigned v) { return __hip_atomic_fetch_add(p, v, __ATOMIC_RELAXED, __HIP_MEMORY_SCOPE_AGENT); }
; #define XB_SPIN(cond, bar) do { unsigned _sp = 0; while (cond) { __builtin_amdgcn_s_sleep(1); \
;     if ((++_sp & 255u) == 0u) { if (xb_ld(&(bar)[XB_TMO])) break; if (_sp > XB_SPIN_CAP) { atomicAdd(&(bar)[XB_TMO], 1u); break; } } } } while (0)
; __device__ __forceinline__ void xcd_barrier(const XcdBarrier& b) {
;     asm volatile("s_waitcnt vmcnt(0)" ::: "memory");
;     __syncthreads();
;     if (threadIdx.x == 0) {
;         unsigned* bar = b.bar;
;         __builtin_amdgcn_s_waitcnt(0);
;         unsigned nloc = b.st[0], nx = b.st[1];
;         if (nloc == 0u) { xcd_barrier_complete(bar, b.x, b.total, nloc, nx); b.st[0] = nloc; b.st[1] = nx; }
;         const unsigned old = xb_add(&bar[XB_XSUB(b.x)], 1u);
;         const unsigned gen = old / nloc;
;         if (old + 1u == (gen + 1u) * nloc) {
;             __builtin_amdgcn_fence(__ATOMIC_RELEASE, "agent");
;             asm volatile("s_waitcnt vmcnt(0)" ::: "memory");
;             const unsigned og = xb_add(&bar[XB_TOP], 1u);
;             const unsigned tg = og / nx;
;             if (og + 1u == (tg + 1u) * nx) xb_add(&bar[XB_TOPGEN], 1u);
;             else XB_SPIN(xb_ld(&bar[XB_TOPGEN]) == tg, bar);
;             __builtin_amdgcn_fence(__ATOMIC_ACQUIRE, "agent");
;             xb_add(&bar[XB_XGEN(b.x)], 1u);
;             asm volatile("s_waitcnt vmcnt(0)" ::: "memory");
;         } else {
;             XB_SPIN(xb_ld(&bar[XB_XGEN(b.x)]) == gen, bar);
.LBB0_652:
	s_or_b64 exec, exec, s[8:9]
	v_cvt_f32_u32_e32 v5, v3
	s_waitcnt vmcnt(0)
	v_readfirstlane_b32 s0, v4
	v_sub_u32_e32 v4, 0, v3
	v_rcp_iflag_f32_e32 v5, v5
	v_add_u32_e32 v6, s0, v2
	v_mul_f32_e32 v5, 0x4f7ffffe, v5
	v_cvt_u32_f32_e32 v5, v5
	v_mul_lo_u32 v2, v4, v5
	v_mul_hi_u32 v2, v5, v2
	v_add_u32_e32 v2, v5, v2
	v_mul_hi_u32 v2, v6, v2
	v_mul_lo_u32 v4, v2, v3
	v_sub_u32_e32 v4, v6, v4
	v_add_u32_e32 v5, 1, v2
	v_cmp_ge_u32_e32 vcc, v4, v3
	s_nop 1
	v_cndmask_b32_e32 v2, v2, v5, vcc
	v_sub_u32_e32 v5, v4, v3
	v_cndmask_b32_e32 v4, v4, v5, vcc
	v_add_u32_e32 v5, 1, v2
	v_cmp_ge_u32_e32 vcc, v4, v3
	v_add_u32_e32 v4, 1, v6
	s_nop 0
	v_cndmask_b32_e32 v2, v2, v5, vcc
	v_mul_lo_u32 v5, v3, v2
	v_add_u32_e32 v3, v5, v3
	v_cmp_ne_u32_e32 vcc, v4, v3
	s_and_saveexec_b64 s[0:1], vcc
	s_xor_b64 s[8:9], exec, s[0:1]
	s_cbranch_execz .LBB0_666
	s_waitcnt lgkmcnt(0)
	v_add_u32_e32 v4, 1, v2
	v_mul_lo_u32 v4, v4, v1
	v_mov_b32_e32 v1, 0x3000
	global_load_dword v1, v1, s[42:43] offset:1024 sc1
	s_add_u32 s10, s42, 0x3400
	s_addc_u32 s11, s43, 0
	s_waitcnt vmcnt(0)
	v_cmp_lt_u32_e32 vcc, v1, v4
	s_and_saveexec_b64 s[0:1], vcc
	s_cbranch_execz .LBB0_665
	s_mov_b32 s22, 1
	s_mov_b64 s[12:13], 0
	v_mov_b32_e32 v1, 0
	s_branch .LBB0_656

; __device__ __forceinline__ unsigned xb_ld(unsigned* p)              { return __hip_atomic_load(p, __ATOMIC_RELAXED, __HIP_MEMORY_SCOPE_AGENT); }
; #define XB_SPIN(cond, bar) do { unsigned _sp = 0; while (cond) { __builtin_amdgcn_s_sleep(1); \
;     if ((++_sp & 255u) == 0u) { if (xb_ld(&(bar)[XB_TMO])) break; if (_sp > XB_SPIN_CAP) { atomicAdd(&(bar)[XB_TMO], 1u); break; } } } } while (0)
; __device__ __forceinline__ void xcd_barrier(const XcdBarrier& b) {
;     ...
;             XB_SPIN(xb_ld(&bar[XB_XGEN(b.x)]) == gen, bar);
.LBB0_658:
	global_load_dword v3, v1, s[10:11] sc1
	s_add_i32 s22, s22, 1
	s_mov_b64 s[18:19], -1
	s_waitcnt vmcnt(0)
	v_cmp_ge_u32_e32 vcc, v3, v4
	s_orn2_b64 s[16:17], vcc, exec
	s_branch .LBB0_655

; __device__ __forceinline__ unsigned xb_ld(unsigned* p)              { return __hip_atomic_load(p, __ATOMIC_RELAXED, __HIP_MEMORY_SCOPE_AGENT); }
; __device__ __forceinline__ unsigned xb_add(unsigned* p, unsigned v) { return __hip_atomic_fetch_add(p, v, __ATOMIC_RELAXED, __HIP_MEMORY_SCOPE_AGENT); }
; #define XB_SPIN(cond, bar) do { unsigned _sp = 0; while (cond) { __builtin_amdgcn_s_sleep(1); \
;     if ((++_sp & 255u) == 0u) { if (xb_ld(&(bar)[XB_TMO])) break; if (_sp > XB_SPIN_CAP) { atomicAdd(&(bar)[XB_TMO], 1u); break; } } } } while (0)
; __device__ __forceinline__ void xcd_barrier(const XcdBarrier& b) {
;     ...
;         if (old + 1u == (gen + 1u) * nloc) {
;             __builtin_amdgcn_fence(__ATOMIC_RELEASE, "agent");
;             asm volatile("s_waitcnt vmcnt(0)" ::: "memory");
;             const unsigned og = xb_add(&bar[XB_TOP], 1u);
;             const unsigned tg = og / nx;
;             if (og + 1u == (tg + 1u) * nx) xb_add(&bar[XB_TOPGEN], 1u);
;             else XB_SPIN(xb_ld(&bar[XB_TOPGEN]) == tg, bar);
;             __builtin_amdgcn_fence(__ATOMIC_ACQUIRE, "agent");
;             xb_add(&bar[XB_XGEN(b.x)], 1u);
.LBB0_666:
	s_andn2_saveexec_b64 s[0:1], s[8:9]
	s_cbranch_execz .LBB0_686
	s_mov_b64 s[0:1], exec
	v_add_u32_e32 v7, 1, v2
	buffer_wbl2 sc1
	s_waitcnt lgkmcnt(0)
	v_mul_lo_u32 v7, v7, v1
	s_waitcnt vmcnt(0)
	v_mbcnt_lo_u32_b32 v2, s0, 0
	v_mbcnt_hi_u32_b32 v2, s1, v2
	v_cmp_eq_u32_e32 vcc, 0, v2
	s_and_saveexec_b64 s[8:9], vcc
	s_cbranch_execz .LBB0_669
	s_bcnt1_i32_b64 s0, s[0:1]
	v_mov_b32_e32 v3, 0x3000
	v_mov_b32_e32 v4, s0
	global_atomic_add v3, v4, s[42:43] offset:1024
.LBB0_669:
	s_or_b64 exec, exec, s[8:9]
	v_mov_b32_e32 v1, 0
	v_mov_b32_e32 v5, 0
	s_add_u32 s0, s42, 0x3400
	s_addc_u32 s1, s43, 0

; __device__ __forceinline__ unsigned xb_ld(unsigned* p)              { return __hip_atomic_load(p, __ATOMIC_RELAXED, __HIP_MEMORY_SCOPE_AGENT); }
; __device__ __forceinline__ unsigned xb_add(unsigned* p, unsigned v) { return __hip_atomic_fetch_add(p, v, __ATOMIC_RELAXED, __HIP_MEMORY_SCOPE_AGENT); }
; #define XB_SPIN(cond, bar) do { unsigned _sp = 0; while (cond) { __builtin_amdgcn_s_sleep(1); \
;     if ((++_sp & 255u) == 0u) { if (xb_ld(&(bar)[XB_TMO])) break; if (_sp > XB_SPIN_CAP) { atomicAdd(&(bar)[XB_TMO], 1u); break; } } } } while (0)
; __device__ __forceinline__ void xcd_barrier(const XcdBarrier& b) {
;     ...
;         const unsigned old = xb_add(&bar[XB_XSUB(b.x)], 1u);
;         const unsigned gen = old / nloc;
;         if (old + 1u == (gen + 1u) * nloc) {
;             __builtin_amdgcn_fence(__ATOMIC_RELEASE, "agent");
;             asm volatile("s_waitcnt vmcnt(0)" ::: "memory");
;             const unsigned og = xb_add(&bar[XB_TOP], 1u);
;             const unsigned tg = og / nx;
;             if (og + 1u == (tg + 1u) * nx) xb_add(&bar[XB_TOPGEN], 1u);
;             else XB_SPIN(xb_ld(&bar[XB_TOPGEN]) == tg, bar);
.LBB0_727:
	s_or_b64 exec, exec, s[10:11]
	v_cvt_f32_u32_e32 v5, v3
	s_waitcnt vmcnt(0)
	v_readfirstlane_b32 s0, v4
	v_sub_u32_e32 v4, 0, v3
	v_rcp_iflag_f32_e32 v5, v5
	v_add_u32_e32 v6, s0, v2
	v_mul_f32_e32 v5, 0x4f7ffffe, v5
	v_cvt_u32_f32_e32 v5, v5
	v_mul_lo_u32 v2, v4, v5
	v_mul_hi_u32 v2, v5, v2
	v_add_u32_e32 v2, v5, v2
	v_mul_hi_u32 v2, v6, v2
	v_mul_lo_u32 v4, v2, v3
	v_sub_u32_e32 v4, v6, v4
	v_add_u32_e32 v5, 1, v2
	v_cmp_ge_u32_e32 vcc, v4, v3
	s_nop 1
	v_cndmask_b32_e32 v2, v2, v5, vcc
	v_sub_u32_e32 v5, v4, v3
	v_cndmask_b32_e32 v4, v4, v5, vcc
	v_add_u32_e32 v5, 1, v2
	v_cmp_ge_u32_e32 vcc, v4, v3
	v_add_u32_e32 v4, 1, v6
	s_nop 0
	v_cndmask_b32_e32 v2, v2, v5, vcc
	v_mul_lo_u32 v5, v3, v2
	v_add_u32_e32 v3, v5, v3
	v_cmp_ne_u32_e32 vcc, v4, v3
	s_and_saveexec_b64 s[0:1], vcc
	s_xor_b64 s[10:11], exec, s[0:1]
	s_cbranch_execz .LBB0_741
	s_waitcnt lgkmcnt(0)
	v_add_u32_e32 v4, 1, v2
	v_mul_lo_u32 v4, v4, v1
	v_mov_b32_e32 v1, 0x3000
	global_load_dword v1, v1, s[42:43] offset:1024 sc1
	s_add_u32 s12, s42, 0x3400
	s_addc_u32 s13, s43, 0
	s_waitcnt vmcnt(0)
	v_cmp_lt_u32_e32 vcc, v1, v4
	s_and_saveexec_b64 s[0:1], vcc
	s_cbranch_execz .LBB0_740
	s_mov_b32 s24, 1
	s_mov_b64 s[14:15], 0
	v_mov_b32_e32 v1, 0
	s_branch .LBB0_731

; __device__ __forceinline__ unsigned xb_ld(unsigned* p)              { return __hip_atomic_load(p, __ATOMIC_RELAXED, __HIP_MEMORY_SCOPE_AGENT); }
; __device__ __forceinline__ unsigned xb_add(unsigned* p, unsigned v) { return __hip_atomic_fetch_add(p, v, __ATOMIC_RELAXED, __HIP_MEMORY_SCOPE_AGENT); }
; #define XB_SPIN(cond, bar) do { unsigned _sp = 0; while (cond) { __builtin_amdgcn_s_sleep(1); \
;     if ((++_sp & 255u) == 0u) { if (xb_ld(&(bar)[XB_TMO])) break; if (_sp > XB_SPIN_CAP) { atomicAdd(&(bar)[XB_TMO], 1u); break; } } } } while (0)
; __device__ __forceinline__ void xcd_barrier(const XcdBarrier& b) {
;     ...
;             const unsigned og = xb_add(&bar[XB_TOP], 1u);
;             const unsigned tg = og / nx;
;             if (og + 1u == (tg + 1u) * nx) xb_add(&bar[XB_TOPGEN], 1u);
;             else XB_SPIN(xb_ld(&bar[XB_TOPGEN]) == tg, bar);
.LBB0_733:
	global_load_dword v3, v1, s[12:13] sc1
	s_add_i32 s24, s24, 1
	s_mov_b64 s[20:21], -1
	s_waitcnt vmcnt(0)
	v_cmp_ge_u32_e32 vcc, v3, v4
	s_orn2_b64 s[18:19], vcc, exec
	s_branch .LBB0_730
